# lean attention loop with the LDS staging writes and global loads spread over the whole tile
# baseline (speedup 1.0000x reference)
.Lattn_pa0:
	s_waitcnt lgkmcnt(6)
	v_mfma_f32_16x16x32_bf16 v[64:67], v[160:163], v[96:99], 0
	v_exp_f32_e32 v88, v88
	v_mfma_f32_16x16x32_bf16 v[68:71], v[160:163], v[112:115], 0
	v_exp_f32_e32 v92, v92
	ds_read_b128 v[160:163], v201 offset:20480
	s_add_u32 s16, s22, s10
	s_addc_u32 s17, s23, s11
	s_add_u32 s15, s22, s12
	s_addc_u32 s14, s23, s13
	s_add_u32 s8, s16, 0x3bc00200
	s_addc_u32 s9, s17, 0
	s_add_u32 s6, s15, 0x23a50000
	s_addc_u32 s7, s14, 0
	v_mfma_f32_16x16x32_bf16 v[0:3], v[164:167], v[216:219], v[0:3]
	v_cvt_pk_bf16_f32 v242, v80, v81
	v_mfma_f32_16x16x32_bf16 v[4:7], v[164:167], v[238:241], v[4:7]
	v_exp_f32_e32 v89, v89
	ds_read_b128 v[164:167], v209 offset:8192
	s_waitcnt vmcnt(4)
	ds_write_b128 v225, v[152:155] offset:49152
	s_waitcnt lgkmcnt(7)
	v_mfma_f32_16x16x32_bf16 v[68:71], v[168:171], v[116:119], v[68:71]
	v_exp_f32_e32 v93, v93
	v_mfma_f32_16x16x32_bf16 v[64:67], v[168:171], v[100:103], v[64:67]
	v_cvt_pk_bf16_f32 v243, v82, v83
	ds_read_b128 v[168:171], v202 offset:20480
	v_mfma_f32_16x16x32_bf16 v[12:15], v[172:175], v[238:241], v[12:15]
	v_exp_f32_e32 v90, v90
	v_mfma_f32_16x16x32_bf16 v[8:11], v[172:175], v[216:219], v[8:11]
	v_exp_f32_e32 v94, v94
	ds_read_b128 v[172:175], v209 offset:10240
	s_waitcnt lgkmcnt(7)
	v_mfma_f32_16x16x32_bf16 v[64:67], v[176:179], v[104:107], v[64:67]
	v_cvt_pk_bf16_f32 v204, v84, v85
	v_mfma_f32_16x16x32_bf16 v[68:71], v[176:179], v[120:123], v[68:71]
	v_exp_f32_e32 v91, v91
	ds_read_b128 v[176:179], v203 offset:20480
	ds_write_b128 v226, v[156:159] offset:49152
	v_mfma_f32_16x16x32_bf16 v[16:19], v[180:183], v[216:219], v[16:19]
	v_exp_f32_e32 v95, v95
	v_mfma_f32_16x16x32_bf16 v[20:23], v[180:183], v[238:241], v[20:23]
	v_cvt_pk_bf16_f32 v205, v86, v87
	v_add_f32_e32 v220, v220, v88
	ds_read_b128 v[180:183], v209 offset:12288
	s_waitcnt lgkmcnt(8)
	v_mfma_f32_16x16x32_bf16 v[68:71], v[230:233], v[124:127], v[68:71]
	v_add_f32_e32 v221, v221, v92
	v_add_f32_e32 v220, v220, v89
	v_mfma_f32_16x16x32_bf16 v[64:67], v[230:233], v[108:111], v[64:67]
	v_add_f32_e32 v221, v221, v93
	v_cvt_pk_bf16_f32 v244, v88, v89
	ds_read_b128 v[230:233], v246 offset:20480
	v_mfma_f32_16x16x32_bf16 v[28:31], v[234:237], v[238:241], v[28:31]
	v_cvt_pk_bf16_f32 v245, v90, v91
	v_cvt_pk_bf16_f32 v206, v92, v93
	v_mfma_f32_16x16x32_bf16 v[24:27], v[234:237], v[216:219], v[24:27]
	v_cvt_pk_bf16_f32 v207, v94, v95
	ds_read_b128 v[234:237], v209 offset:14336
	ds_write_b64 v227, v[132:133] offset:32768
	s_waitcnt lgkmcnt(9)
	v_mfma_f32_16x16x32_bf16 v[72:75], v[160:163], v[96:99], 0
	v_add_f32_e32 v220, v220, v90
	v_add_f32_e32 v221, v221, v94
	v_mfma_f32_16x16x32_bf16 v[76:79], v[160:163], v[112:115], 0
	v_add_f32_e32 v220, v220, v91
	v_add_f32_e32 v221, v221, v95
	ds_read_b128 v[160:163], v201 offset:24576
	v_mfma_f32_16x16x32_bf16 v[32:35], v[164:167], v[216:219], v[32:35]
	v_add_f32_e32 v194, v194, v220
	v_add_f32_e32 v195, v195, v221
	v_mfma_f32_16x16x32_bf16 v[36:39], v[164:167], v[238:241], v[36:39]
	v_exp_f32_e32 v64, v64
	ds_read_b128 v[164:167], v210 offset:0
	s_waitcnt lgkmcnt(8)
	v_mfma_f32_16x16x32_bf16 v[76:79], v[168:171], v[116:119], v[76:79]
	v_exp_f32_e32 v68, v68
	v_mfma_f32_16x16x32_bf16 v[72:75], v[168:171], v[100:103], v[72:75]
	v_exp_f32_e32 v65, v65
	ds_read_b128 v[168:171], v202 offset:24576
	ds_write_b64 v228, v[134:135] offset:32768
	v_mfma_f32_16x16x32_bf16 v[44:47], v[172:175], v[238:241], v[44:47]
	v_exp_f32_e32 v69, v69
	v_mfma_f32_16x16x32_bf16 v[40:43], v[172:175], v[216:219], v[40:43]
	v_exp_f32_e32 v66, v66
	ds_read_b128 v[172:175], v210 offset:2048
	s_waitcnt lgkmcnt(8)
	v_mfma_f32_16x16x32_bf16 v[72:75], v[176:179], v[104:107], v[72:75]
	v_exp_f32_e32 v70, v70
	v_mfma_f32_16x16x32_bf16 v[76:79], v[176:179], v[120:123], v[76:79]
	v_exp_f32_e32 v67, v67
	ds_read_b128 v[176:179], v203 offset:24576
	v_mfma_f32_16x16x32_bf16 v[48:51], v[180:183], v[216:219], v[48:51]
	v_exp_f32_e32 v71, v71
	v_mfma_f32_16x16x32_bf16 v[52:55], v[180:183], v[238:241], v[52:55]
	v_add_f32_e32 v220, v64, v65
	ds_read_b128 v[180:183], v210 offset:4096
	ds_write_b64 v229, v[128:129] offset:32768
	s_waitcnt lgkmcnt(9)
	v_mfma_f32_16x16x32_bf16 v[76:79], v[230:233], v[124:127], v[76:79]
	v_add_f32_e32 v221, v68, v69
	v_mfma_f32_16x16x32_bf16 v[72:75], v[230:233], v[108:111], v[72:75]
	v_add_f32_e32 v220, v220, v66
	ds_read_b128 v[230:233], v246 offset:24576
	v_mfma_f32_16x16x32_bf16 v[60:63], v[234:237], v[238:241], v[60:63]
	v_add_f32_e32 v221, v221, v70
	v_add_f32_e32 v220, v220, v67
	v_mfma_f32_16x16x32_bf16 v[56:59], v[234:237], v[216:219], v[56:59]
	v_add_f32_e32 v221, v221, v71
	ds_read_b128 v[234:237], v210 offset:6144
	s_waitcnt lgkmcnt(8)
	v_mfma_f32_16x16x32_bf16 v[80:83], v[160:163], v[96:99], 0
	v_exp_f32_e32 v72, v72
	v_mfma_f32_16x16x32_bf16 v[84:87], v[160:163], v[112:115], 0
	v_exp_f32_e32 v76, v76
	ds_read_b128 v[160:163], v201 offset:28672
	ds_write_b64 v184, v[130:131] offset:32768
	v_mfma_f32_16x16x32_bf16 v[0:3], v[164:167], v[242:245], v[0:3]
	v_exp_f32_e32 v73, v73
	v_mfma_f32_16x16x32_bf16 v[4:7], v[164:167], v[204:207], v[4:7]
	v_exp_f32_e32 v77, v77
	ds_read_b128 v[164:167], v210 offset:8192
	s_waitcnt lgkmcnt(8)
	v_mfma_f32_16x16x32_bf16 v[84:87], v[168:171], v[116:119], v[84:87]
	v_exp_f32_e32 v74, v74
	v_mfma_f32_16x16x32_bf16 v[80:83], v[168:171], v[100:103], v[80:83]
	v_exp_f32_e32 v78, v78
	ds_read_b128 v[168:171], v202 offset:28672
	v_mfma_f32_16x16x32_bf16 v[12:15], v[172:175], v[204:207], v[12:15]
	v_exp_f32_e32 v75, v75
	v_mfma_f32_16x16x32_bf16 v[8:11], v[172:175], v[242:245], v[8:11]
	v_exp_f32_e32 v79, v79
	ds_read_b128 v[172:175], v210 offset:10240
	global_load_dwordx4 v[132:135], v198, s[8:9]
	s_waitcnt lgkmcnt(8)
	v_mfma_f32_16x16x32_bf16 v[80:83], v[176:179], v[104:107], v[80:83]
	v_add_f32_e32 v220, v220, v72
	v_add_f32_e32 v221, v221, v76
	v_mfma_f32_16x16x32_bf16 v[84:87], v[176:179], v[120:123], v[84:87]
	v_add_f32_e32 v220, v220, v73
	ds_read_b128 v[176:179], v203 offset:28672
	v_mfma_f32_16x16x32_bf16 v[16:19], v[180:183], v[242:245], v[16:19]
	v_add_f32_e32 v221, v221, v77
	v_add_f32_e32 v220, v220, v74
	v_mfma_f32_16x16x32_bf16 v[20:23], v[180:183], v[204:207], v[20:23]
	v_add_f32_e32 v221, v221, v78
	ds_read_b128 v[180:183], v210 offset:12288
	s_waitcnt lgkmcnt(7)
	v_mfma_f32_16x16x32_bf16 v[84:87], v[230:233], v[124:127], v[84:87]
	v_add_f32_e32 v220, v220, v75
	v_add_f32_e32 v221, v221, v79
	v_mfma_f32_16x16x32_bf16 v[80:83], v[230:233], v[108:111], v[80:83]
	v_cvt_pk_bf16_f32 v216, v64, v65
	ds_read_b128 v[230:233], v246 offset:28672
	global_load_dwordx4 v[128:131], v199, s[8:9]
	v_mfma_f32_16x16x32_bf16 v[28:31], v[234:237], v[204:207], v[28:31]
	v_cvt_pk_bf16_f32 v217, v66, v67
	v_cvt_pk_bf16_f32 v238, v68, v69
	v_mfma_f32_16x16x32_bf16 v[24:27], v[234:237], v[242:245], v[24:27]
	v_cvt_pk_bf16_f32 v239, v70, v71
	ds_read_b128 v[234:237], v210 offset:14336
	s_waitcnt lgkmcnt(6)
	v_mfma_f32_16x16x32_bf16 v[88:91], v[160:163], v[96:99], 0
	v_exp_f32_e32 v80, v80
	v_mfma_f32_16x16x32_bf16 v[92:95], v[160:163], v[112:115], 0
	v_exp_f32_e32 v84, v84
	ds_read_b128 v[160:163], v201 offset:32768
	v_mfma_f32_16x16x32_bf16 v[32:35], v[164:167], v[242:245], v[32:35]
	v_exp_f32_e32 v81, v81
	v_mfma_f32_16x16x32_bf16 v[36:39], v[164:167], v[204:207], v[36:39]
	v_exp_f32_e32 v85, v85
	ds_read_b128 v[164:167], v209 offset:16384
	global_load_dwordx4 v[152:155], v196, s[6:7]
	s_waitcnt lgkmcnt(6)
	v_mfma_f32_16x16x32_bf16 v[92:95], v[168:171], v[116:119], v[92:95]
	v_exp_f32_e32 v82, v82
	v_mfma_f32_16x16x32_bf16 v[88:91], v[168:171], v[100:103], v[88:91]
	v_exp_f32_e32 v86, v86
	ds_read_b128 v[168:171], v202 offset:32768
	v_mfma_f32_16x16x32_bf16 v[44:47], v[172:175], v[204:207], v[44:47]
	v_exp_f32_e32 v83, v83
	v_mfma_f32_16x16x32_bf16 v[40:43], v[172:175], v[242:245], v[40:43]
	v_exp_f32_e32 v87, v87
	ds_read_b128 v[172:175], v209 offset:18432
	s_waitcnt lgkmcnt(6)
	v_mfma_f32_16x16x32_bf16 v[88:91], v[176:179], v[104:107], v[88:91]
	v_add_f32_e32 v220, v220, v80
	v_add_f32_e32 v221, v221, v84
	v_mfma_f32_16x16x32_bf16 v[92:95], v[176:179], v[120:123], v[92:95]
	v_add_f32_e32 v220, v220, v81
	ds_read_b128 v[176:179], v203 offset:32768
	global_load_dwordx4 v[156:159], v197, s[6:7]
	v_mfma_f32_16x16x32_bf16 v[48:51], v[180:183], v[242:245], v[48:51]
	v_add_f32_e32 v221, v221, v85
	v_add_f32_e32 v220, v220, v82
	v_mfma_f32_16x16x32_bf16 v[52:55], v[180:183], v[204:207], v[52:55]
	v_add_f32_e32 v221, v221, v86
	ds_read_b128 v[180:183], v209 offset:20480
	s_waitcnt lgkmcnt(6)
	v_mfma_f32_16x16x32_bf16 v[92:95], v[230:233], v[124:127], v[92:95]
	v_add_f32_e32 v220, v220, v83
	v_add_f32_e32 v221, v221, v87
	v_mfma_f32_16x16x32_bf16 v[88:91], v[230:233], v[108:111], v[88:91]
	v_cvt_pk_bf16_f32 v218, v72, v73
	ds_read_b128 v[230:233], v246 offset:32768
	v_mfma_f32_16x16x32_bf16 v[60:63], v[234:237], v[204:207], v[60:63]
	v_cvt_pk_bf16_f32 v219, v74, v75
	v_cvt_pk_bf16_f32 v240, v76, v77
	v_mfma_f32_16x16x32_bf16 v[56:59], v[234:237], v[242:245], v[56:59]
	v_cvt_pk_bf16_f32 v241, v78, v79
	ds_read_b128 v[234:237], v209 offset:22528
	s_setprio 0
	s_waitcnt lgkmcnt(6)
	v_mfma_f32_16x16x32_bf16 v[64:67], v[160:163], v[96:99], 0
	v_exp_f32_e32 v88, v88
	v_mfma_f32_16x16x32_bf16 v[68:71], v[160:163], v[112:115], 0
	v_exp_f32_e32 v92, v92
	ds_read_b128 v[160:163], v201 offset:36864
	s_add_u32 s8, s16, 0x3bc00280
	s_addc_u32 s9, s17, 0
	s_add_u32 s6, s15, 0x23a60000
	s_addc_u32 s7, s14, 0
	v_mfma_f32_16x16x32_bf16 v[0:3], v[164:167], v[216:219], v[0:3]
	v_cvt_pk_bf16_f32 v242, v80, v81
	v_mfma_f32_16x16x32_bf16 v[4:7], v[164:167], v[238:241], v[4:7]
	v_exp_f32_e32 v89, v89
	ds_read_b128 v[164:167], v209 offset:24576
	s_waitcnt vmcnt(4)
	ds_write_b128 v225, v[136:139] offset:0
	s_waitcnt lgkmcnt(7)
	v_mfma_f32_16x16x32_bf16 v[68:71], v[168:171], v[116:119], v[68:71]
	v_exp_f32_e32 v93, v93
	v_mfma_f32_16x16x32_bf16 v[64:67], v[168:171], v[100:103], v[64:67]
	v_cvt_pk_bf16_f32 v243, v82, v83
	ds_read_b128 v[168:171], v202 offset:36864
	v_mfma_f32_16x16x32_bf16 v[12:15], v[172:175], v[238:241], v[12:15]
	v_exp_f32_e32 v90, v90
	v_mfma_f32_16x16x32_bf16 v[8:11], v[172:175], v[216:219], v[8:11]
	v_exp_f32_e32 v94, v94
	ds_read_b128 v[172:175], v209 offset:26624
	s_waitcnt lgkmcnt(7)
	v_mfma_f32_16x16x32_bf16 v[64:67], v[176:179], v[104:107], v[64:67]
	v_cvt_pk_bf16_f32 v204, v84, v85
	v_mfma_f32_16x16x32_bf16 v[68:71], v[176:179], v[120:123], v[68:71]
	v_exp_f32_e32 v91, v91
	ds_read_b128 v[176:179], v203 offset:36864
	ds_write_b128 v226, v[140:143] offset:0
	v_mfma_f32_16x16x32_bf16 v[16:19], v[180:183], v[216:219], v[16:19]
	v_exp_f32_e32 v95, v95
	v_mfma_f32_16x16x32_bf16 v[20:23], v[180:183], v[238:241], v[20:23]
	v_cvt_pk_bf16_f32 v205, v86, v87
	v_add_f32_e32 v220, v220, v88
	ds_read_b128 v[180:183], v209 offset:28672
	s_waitcnt lgkmcnt(8)
	v_mfma_f32_16x16x32_bf16 v[68:71], v[230:233], v[124:127], v[68:71]
	v_add_f32_e32 v221, v221, v92
	v_add_f32_e32 v220, v220, v89
	v_mfma_f32_16x16x32_bf16 v[64:67], v[230:233], v[108:111], v[64:67]
	v_add_f32_e32 v221, v221, v93
	v_cvt_pk_bf16_f32 v244, v88, v89
	ds_read_b128 v[230:233], v246 offset:36864
	v_mfma_f32_16x16x32_bf16 v[28:31], v[234:237], v[238:241], v[28:31]
	v_cvt_pk_bf16_f32 v245, v90, v91
	v_cvt_pk_bf16_f32 v206, v92, v93
	v_mfma_f32_16x16x32_bf16 v[24:27], v[234:237], v[216:219], v[24:27]
	v_cvt_pk_bf16_f32 v207, v94, v95
	ds_read_b128 v[234:237], v209 offset:30720
	ds_write_b64 v227, v[148:149] offset:49152
	s_waitcnt lgkmcnt(9)
	v_mfma_f32_16x16x32_bf16 v[72:75], v[160:163], v[96:99], 0
	v_add_f32_e32 v220, v220, v90
	v_add_f32_e32 v221, v221, v94
	v_mfma_f32_16x16x32_bf16 v[76:79], v[160:163], v[112:115], 0
	v_add_f32_e32 v220, v220, v91
	v_add_f32_e32 v221, v221, v95
	ds_read_b128 v[160:163], v201 offset:40960
	v_mfma_f32_16x16x32_bf16 v[32:35], v[164:167], v[216:219], v[32:35]
	v_add_f32_e32 v194, v194, v220
	v_add_f32_e32 v195, v195, v221
	v_mfma_f32_16x16x32_bf16 v[36:39], v[164:167], v[238:241], v[36:39]
	v_exp_f32_e32 v64, v64
	ds_read_b128 v[164:167], v210 offset:16384
	s_waitcnt lgkmcnt(8)
	v_mfma_f32_16x16x32_bf16 v[76:79], v[168:171], v[116:119], v[76:79]
	v_exp_f32_e32 v68, v68
	v_mfma_f32_16x16x32_bf16 v[72:75], v[168:171], v[100:103], v[72:75]
	v_exp_f32_e32 v65, v65
	ds_read_b128 v[168:171], v202 offset:40960
	ds_write_b64 v228, v[150:151] offset:49152
	v_mfma_f32_16x16x32_bf16 v[44:47], v[172:175], v[238:241], v[44:47]
	v_exp_f32_e32 v69, v69
	v_mfma_f32_16x16x32_bf16 v[40:43], v[172:175], v[216:219], v[40:43]
	v_exp_f32_e32 v66, v66
	ds_read_b128 v[172:175], v210 offset:18432
	s_waitcnt lgkmcnt(8)
	v_mfma_f32_16x16x32_bf16 v[72:75], v[176:179], v[104:107], v[72:75]
	v_exp_f32_e32 v70, v70
	v_mfma_f32_16x16x32_bf16 v[76:79], v[176:179], v[120:123], v[76:79]
	v_exp_f32_e32 v67, v67
	ds_read_b128 v[176:179], v203 offset:40960
	v_mfma_f32_16x16x32_bf16 v[48:51], v[180:183], v[216:219], v[48:51]
	v_exp_f32_e32 v71, v71
	v_mfma_f32_16x16x32_bf16 v[52:55], v[180:183], v[238:241], v[52:55]
	v_add_f32_e32 v220, v64, v65
	ds_read_b128 v[180:183], v210 offset:20480
	ds_write_b64 v229, v[144:145] offset:49152
	s_waitcnt lgkmcnt(9)
	v_mfma_f32_16x16x32_bf16 v[76:79], v[230:233], v[124:127], v[76:79]
	v_add_f32_e32 v221, v68, v69
	v_mfma_f32_16x16x32_bf16 v[72:75], v[230:233], v[108:111], v[72:75]
	v_add_f32_e32 v220, v220, v66
	ds_read_b128 v[230:233], v246 offset:40960
	v_mfma_f32_16x16x32_bf16 v[60:63], v[234:237], v[238:241], v[60:63]
	v_add_f32_e32 v221, v221, v70
	v_add_f32_e32 v220, v220, v67
	v_mfma_f32_16x16x32_bf16 v[56:59], v[234:237], v[216:219], v[56:59]
	v_add_f32_e32 v221, v221, v71
	ds_read_b128 v[234:237], v210 offset:22528
	s_waitcnt lgkmcnt(8)
	v_mfma_f32_16x16x32_bf16 v[80:83], v[160:163], v[96:99], 0
	v_exp_f32_e32 v72, v72
	v_mfma_f32_16x16x32_bf16 v[84:87], v[160:163], v[112:115], 0
	v_exp_f32_e32 v76, v76
	ds_read_b128 v[160:163], v201 offset:45056
	ds_write_b64 v184, v[146:147] offset:49152
	v_mfma_f32_16x16x32_bf16 v[0:3], v[164:167], v[242:245], v[0:3]
	v_exp_f32_e32 v73, v73
	v_mfma_f32_16x16x32_bf16 v[4:7], v[164:167], v[204:207], v[4:7]
	v_exp_f32_e32 v77, v77
	ds_read_b128 v[164:167], v210 offset:24576
	s_waitcnt lgkmcnt(8)
	v_mfma_f32_16x16x32_bf16 v[84:87], v[168:171], v[116:119], v[84:87]
	v_exp_f32_e32 v74, v74
	v_mfma_f32_16x16x32_bf16 v[80:83], v[168:171], v[100:103], v[80:83]
	v_exp_f32_e32 v78, v78
	ds_read_b128 v[168:171], v202 offset:45056
	v_mfma_f32_16x16x32_bf16 v[12:15], v[172:175], v[204:207], v[12:15]
	v_exp_f32_e32 v75, v75
	v_mfma_f32_16x16x32_bf16 v[8:11], v[172:175], v[242:245], v[8:11]
	v_exp_f32_e32 v79, v79
	ds_read_b128 v[172:175], v210 offset:26624
	global_load_dwordx4 v[148:151], v198, s[8:9]
	s_waitcnt lgkmcnt(8)
	v_mfma_f32_16x16x32_bf16 v[80:83], v[176:179], v[104:107], v[80:83]
	v_add_f32_e32 v220, v220, v72
	v_add_f32_e32 v221, v221, v76
	v_mfma_f32_16x16x32_bf16 v[84:87], v[176:179], v[120:123], v[84:87]
	v_add_f32_e32 v220, v220, v73
	ds_read_b128 v[176:179], v203 offset:45056
	v_mfma_f32_16x16x32_bf16 v[16:19], v[180:183], v[242:245], v[16:19]
	v_add_f32_e32 v221, v221, v77
	v_add_f32_e32 v220, v220, v74
	v_mfma_f32_16x16x32_bf16 v[20:23], v[180:183], v[204:207], v[20:23]
	v_add_f32_e32 v221, v221, v78
	ds_read_b128 v[180:183], v210 offset:28672
	s_waitcnt lgkmcnt(7)
	v_mfma_f32_16x16x32_bf16 v[84:87], v[230:233], v[124:127], v[84:87]
	v_add_f32_e32 v220, v220, v75
	v_add_f32_e32 v221, v221, v79
	v_mfma_f32_16x16x32_bf16 v[80:83], v[230:233], v[108:111], v[80:83]
	v_cvt_pk_bf16_f32 v216, v64, v65
	ds_read_b128 v[230:233], v246 offset:45056
	global_load_dwordx4 v[144:147], v199, s[8:9]
	v_mfma_f32_16x16x32_bf16 v[28:31], v[234:237], v[204:207], v[28:31]
	v_cvt_pk_bf16_f32 v217, v66, v67
	v_cvt_pk_bf16_f32 v238, v68, v69
	v_mfma_f32_16x16x32_bf16 v[24:27], v[234:237], v[242:245], v[24:27]
	v_cvt_pk_bf16_f32 v239, v70, v71
	ds_read_b128 v[234:237], v210 offset:30720
	s_waitcnt lgkmcnt(6)
	v_mfma_f32_16x16x32_bf16 v[88:91], v[160:163], v[96:99], 0
	v_exp_f32_e32 v80, v80
	v_mfma_f32_16x16x32_bf16 v[92:95], v[160:163], v[112:115], 0
	v_exp_f32_e32 v84, v84
	v_mfma_f32_16x16x32_bf16 v[32:35], v[164:167], v[242:245], v[32:35]
	v_exp_f32_e32 v81, v81
	v_mfma_f32_16x16x32_bf16 v[36:39], v[164:167], v[204:207], v[36:39]
	v_exp_f32_e32 v85, v85
	global_load_dwordx4 v[136:139], v196, s[6:7]
	s_waitcnt lgkmcnt(4)
	v_mfma_f32_16x16x32_bf16 v[92:95], v[168:171], v[116:119], v[92:95]
	v_exp_f32_e32 v82, v82
	v_mfma_f32_16x16x32_bf16 v[88:91], v[168:171], v[100:103], v[88:91]
	v_exp_f32_e32 v86, v86
	v_mfma_f32_16x16x32_bf16 v[44:47], v[172:175], v[204:207], v[44:47]
	v_exp_f32_e32 v83, v83
	v_mfma_f32_16x16x32_bf16 v[40:43], v[172:175], v[242:245], v[40:43]
	v_exp_f32_e32 v87, v87
	s_waitcnt lgkmcnt(3)
	v_mfma_f32_16x16x32_bf16 v[88:91], v[176:179], v[104:107], v[88:91]
	v_add_f32_e32 v220, v220, v80
	v_add_f32_e32 v221, v221, v84
	v_mfma_f32_16x16x32_bf16 v[92:95], v[176:179], v[120:123], v[92:95]
	v_add_f32_e32 v220, v220, v81
	global_load_dwordx4 v[140:143], v197, s[6:7]
	s_waitcnt lgkmcnt(0)
	s_barrier
	ds_read_b128 v[160:163], v201 offset:49152
	ds_read_b128 v[164:167], v209 offset:32768
	ds_read_b128 v[168:171], v202 offset:49152
	ds_read_b128 v[172:175], v209 offset:34816
	ds_read_b128 v[176:179], v203 offset:49152
	v_mfma_f32_16x16x32_bf16 v[48:51], v[180:183], v[242:245], v[48:51]
	v_add_f32_e32 v221, v221, v85
	v_add_f32_e32 v220, v220, v82
	v_mfma_f32_16x16x32_bf16 v[52:55], v[180:183], v[204:207], v[52:55]
	v_add_f32_e32 v221, v221, v86
	ds_read_b128 v[180:183], v209 offset:36864
	v_mfma_f32_16x16x32_bf16 v[92:95], v[230:233], v[124:127], v[92:95]
	v_add_f32_e32 v220, v220, v83
	v_add_f32_e32 v221, v221, v87
	v_mfma_f32_16x16x32_bf16 v[88:91], v[230:233], v[108:111], v[88:91]
	v_cvt_pk_bf16_f32 v218, v72, v73
	ds_read_b128 v[230:233], v246 offset:49152
	v_mfma_f32_16x16x32_bf16 v[60:63], v[234:237], v[204:207], v[60:63]
	v_cvt_pk_bf16_f32 v219, v74, v75
	v_cvt_pk_bf16_f32 v240, v76, v77
	v_mfma_f32_16x16x32_bf16 v[56:59], v[234:237], v[242:245], v[56:59]
	v_cvt_pk_bf16_f32 v241, v78, v79
	ds_read_b128 v[234:237], v209 offset:38912
	s_cmp_eq_u32 s100, 0
	s_cbranch_scc1 .Lattn_pa2
	s_setprio 1
.Lattn_pa2:
	s_waitcnt lgkmcnt(6)
	v_mfma_f32_16x16x32_bf16 v[64:67], v[160:163], v[96:99], 0
	v_exp_f32_e32 v88, v88
	v_mfma_f32_16x16x32_bf16 v[68:71], v[160:163], v[112:115], 0
	v_exp_f32_e32 v92, v92
	ds_read_b128 v[160:163], v201 offset:53248
	s_add_u32 s8, s16, 0x3bc00300
	s_addc_u32 s9, s17, 0
	s_add_u32 s6, s15, 0x23a70000
	s_addc_u32 s7, s14, 0
	v_mfma_f32_16x16x32_bf16 v[0:3], v[164:167], v[216:219], v[0:3]
	v_cvt_pk_bf16_f32 v242, v80, v81
	v_mfma_f32_16x16x32_bf16 v[4:7], v[164:167], v[238:241], v[4:7]
	v_exp_f32_e32 v89, v89
	ds_read_b128 v[164:167], v209 offset:40960
	s_waitcnt vmcnt(4)
	ds_write_b128 v225, v[152:155] offset:16384
	s_waitcnt lgkmcnt(7)
	v_mfma_f32_16x16x32_bf16 v[68:71], v[168:171], v[116:119], v[68:71]
	v_exp_f32_e32 v93, v93
	v_mfma_f32_16x16x32_bf16 v[64:67], v[168:171], v[100:103], v[64:67]
	v_cvt_pk_bf16_f32 v243, v82, v83
	ds_read_b128 v[168:171], v202 offset:53248
	v_mfma_f32_16x16x32_bf16 v[12:15], v[172:175], v[238:241], v[12:15]
	v_exp_f32_e32 v90, v90
	v_mfma_f32_16x16x32_bf16 v[8:11], v[172:175], v[216:219], v[8:11]
	v_exp_f32_e32 v94, v94
	ds_read_b128 v[172:175], v209 offset:43008
	s_waitcnt lgkmcnt(7)
	v_mfma_f32_16x16x32_bf16 v[64:67], v[176:179], v[104:107], v[64:67]
	v_cvt_pk_bf16_f32 v204, v84, v85
	v_mfma_f32_16x16x32_bf16 v[68:71], v[176:179], v[120:123], v[68:71]
	v_exp_f32_e32 v91, v91
	ds_read_b128 v[176:179], v203 offset:53248
	ds_write_b128 v226, v[156:159] offset:16384
	v_mfma_f32_16x16x32_bf16 v[16:19], v[180:183], v[216:219], v[16:19]
	v_exp_f32_e32 v95, v95
	v_mfma_f32_16x16x32_bf16 v[20:23], v[180:183], v[238:241], v[20:23]
	v_cvt_pk_bf16_f32 v205, v86, v87
	v_add_f32_e32 v220, v220, v88
	ds_read_b128 v[180:183], v209 offset:45056
	s_waitcnt lgkmcnt(8)
	v_mfma_f32_16x16x32_bf16 v[68:71], v[230:233], v[124:127], v[68:71]
	v_add_f32_e32 v221, v221, v92
	v_add_f32_e32 v220, v220, v89
	v_mfma_f32_16x16x32_bf16 v[64:67], v[230:233], v[108:111], v[64:67]
	v_add_f32_e32 v221, v221, v93
	v_cvt_pk_bf16_f32 v244, v88, v89
	ds_read_b128 v[230:233], v246 offset:53248
	v_mfma_f32_16x16x32_bf16 v[28:31], v[234:237], v[238:241], v[28:31]
	v_cvt_pk_bf16_f32 v245, v90, v91
	v_cvt_pk_bf16_f32 v206, v92, v93
	v_mfma_f32_16x16x32_bf16 v[24:27], v[234:237], v[216:219], v[24:27]
	v_cvt_pk_bf16_f32 v207, v94, v95
	ds_read_b128 v[234:237], v209 offset:47104
	ds_write_b64 v227, v[132:133] offset:0
	s_waitcnt lgkmcnt(9)
	v_mfma_f32_16x16x32_bf16 v[72:75], v[160:163], v[96:99], 0
	v_add_f32_e32 v220, v220, v90
	v_add_f32_e32 v221, v221, v94
	v_mfma_f32_16x16x32_bf16 v[76:79], v[160:163], v[112:115], 0
	v_add_f32_e32 v220, v220, v91
	v_add_f32_e32 v221, v221, v95
	ds_read_b128 v[160:163], v201 offset:57344
	v_mfma_f32_16x16x32_bf16 v[32:35], v[164:167], v[216:219], v[32:35]
	v_add_f32_e32 v194, v194, v220
	v_add_f32_e32 v195, v195, v221
	v_mfma_f32_16x16x32_bf16 v[36:39], v[164:167], v[238:241], v[36:39]
	v_exp_f32_e32 v64, v64
	ds_read_b128 v[164:167], v210 offset:32768
	s_waitcnt lgkmcnt(8)
	v_mfma_f32_16x16x32_bf16 v[76:79], v[168:171], v[116:119], v[76:79]
	v_exp_f32_e32 v68, v68
	v_mfma_f32_16x16x32_bf16 v[72:75], v[168:171], v[100:103], v[72:75]
	v_exp_f32_e32 v65, v65
	ds_read_b128 v[168:171], v202 offset:57344
	ds_write_b64 v228, v[134:135] offset:0
	v_mfma_f32_16x16x32_bf16 v[44:47], v[172:175], v[238:241], v[44:47]
	v_exp_f32_e32 v69, v69
	v_mfma_f32_16x16x32_bf16 v[40:43], v[172:175], v[216:219], v[40:43]
	v_exp_f32_e32 v66, v66
	ds_read_b128 v[172:175], v210 offset:34816
	s_waitcnt lgkmcnt(8)
	v_mfma_f32_16x16x32_bf16 v[72:75], v[176:179], v[104:107], v[72:75]
	v_exp_f32_e32 v70, v70
	v_mfma_f32_16x16x32_bf16 v[76:79], v[176:179], v[120:123], v[76:79]
	v_exp_f32_e32 v67, v67
	ds_read_b128 v[176:179], v203 offset:57344
	v_mfma_f32_16x16x32_bf16 v[48:51], v[180:183], v[216:219], v[48:51]
	v_exp_f32_e32 v71, v71
	v_mfma_f32_16x16x32_bf16 v[52:55], v[180:183], v[238:241], v[52:55]
	v_add_f32_e32 v220, v64, v65
	ds_read_b128 v[180:183], v210 offset:36864
	ds_write_b64 v229, v[128:129] offset:0
	s_waitcnt lgkmcnt(9)
	v_mfma_f32_16x16x32_bf16 v[76:79], v[230:233], v[124:127], v[76:79]
	v_add_f32_e32 v221, v68, v69
	v_mfma_f32_16x16x32_bf16 v[72:75], v[230:233], v[108:111], v[72:75]
	v_add_f32_e32 v220, v220, v66
	ds_read_b128 v[230:233], v246 offset:57344
	v_mfma_f32_16x16x32_bf16 v[60:63], v[234:237], v[238:241], v[60:63]
	v_add_f32_e32 v221, v221, v70
	v_add_f32_e32 v220, v220, v67
	v_mfma_f32_16x16x32_bf16 v[56:59], v[234:237], v[216:219], v[56:59]
	v_add_f32_e32 v221, v221, v71
	ds_read_b128 v[234:237], v210 offset:38912
	s_waitcnt lgkmcnt(8)
	v_mfma_f32_16x16x32_bf16 v[80:83], v[160:163], v[96:99], 0
	v_exp_f32_e32 v72, v72
	v_mfma_f32_16x16x32_bf16 v[84:87], v[160:163], v[112:115], 0
	v_exp_f32_e32 v76, v76
	ds_read_b128 v[160:163], v201 offset:61440
	ds_write_b64 v184, v[130:131] offset:0
	v_mfma_f32_16x16x32_bf16 v[0:3], v[164:167], v[242:245], v[0:3]
	v_exp_f32_e32 v73, v73
	v_mfma_f32_16x16x32_bf16 v[4:7], v[164:167], v[204:207], v[4:7]
	v_exp_f32_e32 v77, v77
	ds_read_b128 v[164:167], v210 offset:40960
	s_waitcnt lgkmcnt(8)
	v_mfma_f32_16x16x32_bf16 v[84:87], v[168:171], v[116:119], v[84:87]
	v_exp_f32_e32 v74, v74
	v_mfma_f32_16x16x32_bf16 v[80:83], v[168:171], v[100:103], v[80:83]
	v_exp_f32_e32 v78, v78
	ds_read_b128 v[168:171], v202 offset:61440
	v_mfma_f32_16x16x32_bf16 v[12:15], v[172:175], v[204:207], v[12:15]
	v_exp_f32_e32 v75, v75
	v_mfma_f32_16x16x32_bf16 v[8:11], v[172:175], v[242:245], v[8:11]
	v_exp_f32_e32 v79, v79
	ds_read_b128 v[172:175], v210 offset:43008
	global_load_dwordx4 v[132:135], v198, s[8:9]
	s_waitcnt lgkmcnt(8)
	v_mfma_f32_16x16x32_bf16 v[80:83], v[176:179], v[104:107], v[80:83]
	v_add_f32_e32 v220, v220, v72
	v_add_f32_e32 v221, v221, v76
	v_mfma_f32_16x16x32_bf16 v[84:87], v[176:179], v[120:123], v[84:87]
	v_add_f32_e32 v220, v220, v73
	ds_read_b128 v[176:179], v203 offset:61440
	v_mfma_f32_16x16x32_bf16 v[16:19], v[180:183], v[242:245], v[16:19]
	v_add_f32_e32 v221, v221, v77
	v_add_f32_e32 v220, v220, v74
	v_mfma_f32_16x16x32_bf16 v[20:23], v[180:183], v[204:207], v[20:23]
	v_add_f32_e32 v221, v221, v78
	ds_read_b128 v[180:183], v210 offset:45056
	s_waitcnt lgkmcnt(7)
	v_mfma_f32_16x16x32_bf16 v[84:87], v[230:233], v[124:127], v[84:87]
	v_add_f32_e32 v220, v220, v75
	v_add_f32_e32 v221, v221, v79
	v_mfma_f32_16x16x32_bf16 v[80:83], v[230:233], v[108:111], v[80:83]
	v_cvt_pk_bf16_f32 v216, v64, v65
	ds_read_b128 v[230:233], v246 offset:61440
	global_load_dwordx4 v[128:131], v199, s[8:9]
	v_mfma_f32_16x16x32_bf16 v[28:31], v[234:237], v[204:207], v[28:31]
	v_cvt_pk_bf16_f32 v217, v66, v67
	v_cvt_pk_bf16_f32 v238, v68, v69
	v_mfma_f32_16x16x32_bf16 v[24:27], v[234:237], v[242:245], v[24:27]
	v_cvt_pk_bf16_f32 v239, v70, v71
	ds_read_b128 v[234:237], v210 offset:47104
	s_waitcnt lgkmcnt(6)
	v_mfma_f32_16x16x32_bf16 v[88:91], v[160:163], v[96:99], 0
	v_exp_f32_e32 v80, v80
	v_mfma_f32_16x16x32_bf16 v[92:95], v[160:163], v[112:115], 0
	v_exp_f32_e32 v84, v84
	ds_read_b128 v[160:163], v201 offset:0
	v_mfma_f32_16x16x32_bf16 v[32:35], v[164:167], v[242:245], v[32:35]
	v_exp_f32_e32 v81, v81
	v_mfma_f32_16x16x32_bf16 v[36:39], v[164:167], v[204:207], v[36:39]
	v_exp_f32_e32 v85, v85
	ds_read_b128 v[164:167], v209 offset:49152
	global_load_dwordx4 v[152:155], v196, s[6:7]
	s_waitcnt lgkmcnt(6)
	v_mfma_f32_16x16x32_bf16 v[92:95], v[168:171], v[116:119], v[92:95]
	v_exp_f32_e32 v82, v82
	v_mfma_f32_16x16x32_bf16 v[88:91], v[168:171], v[100:103], v[88:91]
	v_exp_f32_e32 v86, v86
	ds_read_b128 v[168:171], v202 offset:0
	v_mfma_f32_16x16x32_bf16 v[44:47], v[172:175], v[204:207], v[44:47]
	v_exp_f32_e32 v83, v83
	v_mfma_f32_16x16x32_bf16 v[40:43], v[172:175], v[242:245], v[40:43]
	v_exp_f32_e32 v87, v87
	ds_read_b128 v[172:175], v209 offset:51200
	s_waitcnt lgkmcnt(6)
	v_mfma_f32_16x16x32_bf16 v[88:91], v[176:179], v[104:107], v[88:91]
	v_add_f32_e32 v220, v220, v80
	v_add_f32_e32 v221, v221, v84
	v_mfma_f32_16x16x32_bf16 v[92:95], v[176:179], v[120:123], v[92:95]
	v_add_f32_e32 v220, v220, v81
	ds_read_b128 v[176:179], v203 offset:0
	global_load_dwordx4 v[156:159], v197, s[6:7]
	v_mfma_f32_16x16x32_bf16 v[48:51], v[180:183], v[242:245], v[48:51]
	v_add_f32_e32 v221, v221, v85
	v_add_f32_e32 v220, v220, v82
	v_mfma_f32_16x16x32_bf16 v[52:55], v[180:183], v[204:207], v[52:55]
	v_add_f32_e32 v221, v221, v86
	ds_read_b128 v[180:183], v209 offset:53248
	s_waitcnt lgkmcnt(6)
	v_mfma_f32_16x16x32_bf16 v[92:95], v[230:233], v[124:127], v[92:95]
	v_add_f32_e32 v220, v220, v83
	v_add_f32_e32 v221, v221, v87
	v_mfma_f32_16x16x32_bf16 v[88:91], v[230:233], v[108:111], v[88:91]
	v_cvt_pk_bf16_f32 v218, v72, v73
	ds_read_b128 v[230:233], v246 offset:0
	v_mfma_f32_16x16x32_bf16 v[60:63], v[234:237], v[204:207], v[60:63]
	v_cvt_pk_bf16_f32 v219, v74, v75
	v_cvt_pk_bf16_f32 v240, v76, v77
	v_mfma_f32_16x16x32_bf16 v[56:59], v[234:237], v[242:245], v[56:59]
	v_cvt_pk_bf16_f32 v241, v78, v79
	ds_read_b128 v[234:237], v209 offset:55296
	s_setprio 0
	s_waitcnt lgkmcnt(6)
	v_mfma_f32_16x16x32_bf16 v[64:67], v[160:163], v[96:99], 0
	v_exp_f32_e32 v88, v88
	v_mfma_f32_16x16x32_bf16 v[68:71], v[160:163], v[112:115], 0
	v_exp_f32_e32 v92, v92
	ds_read_b128 v[160:163], v201 offset:4096
	s_add_u32 s8, s16, 0x3bc00380
	s_addc_u32 s9, s17, 0
	s_add_u32 s6, s15, 0x23a80000
	s_addc_u32 s7, s14, 0
	v_mfma_f32_16x16x32_bf16 v[0:3], v[164:167], v[216:219], v[0:3]
	v_cvt_pk_bf16_f32 v242, v80, v81
	v_mfma_f32_16x16x32_bf16 v[4:7], v[164:167], v[238:241], v[4:7]
	v_exp_f32_e32 v89, v89
	ds_read_b128 v[164:167], v209 offset:57344
	s_waitcnt vmcnt(4)
	ds_write_b128 v225, v[136:139] offset:32768
	s_waitcnt lgkmcnt(7)
	v_mfma_f32_16x16x32_bf16 v[68:71], v[168:171], v[116:119], v[68:71]
	v_exp_f32_e32 v93, v93
	v_mfma_f32_16x16x32_bf16 v[64:67], v[168:171], v[100:103], v[64:67]
	v_cvt_pk_bf16_f32 v243, v82, v83
	ds_read_b128 v[168:171], v202 offset:4096
	v_mfma_f32_16x16x32_bf16 v[12:15], v[172:175], v[238:241], v[12:15]
	v_exp_f32_e32 v90, v90
	v_mfma_f32_16x16x32_bf16 v[8:11], v[172:175], v[216:219], v[8:11]
	v_exp_f32_e32 v94, v94
	ds_read_b128 v[172:175], v209 offset:59392
	s_waitcnt lgkmcnt(7)
	v_mfma_f32_16x16x32_bf16 v[64:67], v[176:179], v[104:107], v[64:67]
	v_cvt_pk_bf16_f32 v204, v84, v85
	v_mfma_f32_16x16x32_bf16 v[68:71], v[176:179], v[120:123], v[68:71]
	v_exp_f32_e32 v91, v91
	ds_read_b128 v[176:179], v203 offset:4096
	ds_write_b128 v226, v[140:143] offset:32768
	v_mfma_f32_16x16x32_bf16 v[16:19], v[180:183], v[216:219], v[16:19]
	v_exp_f32_e32 v95, v95
	v_mfma_f32_16x16x32_bf16 v[20:23], v[180:183], v[238:241], v[20:23]
	v_cvt_pk_bf16_f32 v205, v86, v87
	v_add_f32_e32 v220, v220, v88
	ds_read_b128 v[180:183], v209 offset:61440
	s_waitcnt lgkmcnt(8)
	v_mfma_f32_16x16x32_bf16 v[68:71], v[230:233], v[124:127], v[68:71]
	v_add_f32_e32 v221, v221, v92
	v_add_f32_e32 v220, v220, v89
	v_mfma_f32_16x16x32_bf16 v[64:67], v[230:233], v[108:111], v[64:67]
	v_add_f32_e32 v221, v221, v93
	v_cvt_pk_bf16_f32 v244, v88, v89
	ds_read_b128 v[230:233], v246 offset:4096
	v_mfma_f32_16x16x32_bf16 v[28:31], v[234:237], v[238:241], v[28:31]
	v_cvt_pk_bf16_f32 v245, v90, v91
	v_cvt_pk_bf16_f32 v206, v92, v93
	v_mfma_f32_16x16x32_bf16 v[24:27], v[234:237], v[216:219], v[24:27]
	v_cvt_pk_bf16_f32 v207, v94, v95
	ds_read_b128 v[234:237], v209 offset:63488
	ds_write_b64 v227, v[148:149] offset:16384
	s_waitcnt lgkmcnt(9)
	v_mfma_f32_16x16x32_bf16 v[72:75], v[160:163], v[96:99], 0
	v_add_f32_e32 v220, v220, v90
	v_add_f32_e32 v221, v221, v94
	v_mfma_f32_16x16x32_bf16 v[76:79], v[160:163], v[112:115], 0
	v_add_f32_e32 v220, v220, v91
	v_add_f32_e32 v221, v221, v95
	ds_read_b128 v[160:163], v201 offset:8192
	v_mfma_f32_16x16x32_bf16 v[32:35], v[164:167], v[216:219], v[32:35]
	v_add_f32_e32 v194, v194, v220
	v_add_f32_e32 v195, v195, v221
	v_mfma_f32_16x16x32_bf16 v[36:39], v[164:167], v[238:241], v[36:39]
	v_exp_f32_e32 v64, v64
	ds_read_b128 v[164:167], v210 offset:49152
	s_waitcnt lgkmcnt(8)
	v_mfma_f32_16x16x32_bf16 v[76:79], v[168:171], v[116:119], v[76:79]
	v_exp_f32_e32 v68, v68
	v_mfma_f32_16x16x32_bf16 v[72:75], v[168:171], v[100:103], v[72:75]
	v_exp_f32_e32 v65, v65
	ds_read_b128 v[168:171], v202 offset:8192
	ds_write_b64 v228, v[150:151] offset:16384
	v_mfma_f32_16x16x32_bf16 v[44:47], v[172:175], v[238:241], v[44:47]
	v_exp_f32_e32 v69, v69
	v_mfma_f32_16x16x32_bf16 v[40:43], v[172:175], v[216:219], v[40:43]
	v_exp_f32_e32 v66, v66
	ds_read_b128 v[172:175], v210 offset:51200
	s_waitcnt lgkmcnt(8)
	v_mfma_f32_16x16x32_bf16 v[72:75], v[176:179], v[104:107], v[72:75]
	v_exp_f32_e32 v70, v70
	v_mfma_f32_16x16x32_bf16 v[76:79], v[176:179], v[120:123], v[76:79]
	v_exp_f32_e32 v67, v67
	ds_read_b128 v[176:179], v203 offset:8192
	v_mfma_f32_16x16x32_bf16 v[48:51], v[180:183], v[216:219], v[48:51]
	v_exp_f32_e32 v71, v71
	v_mfma_f32_16x16x32_bf16 v[52:55], v[180:183], v[238:241], v[52:55]
	v_add_f32_e32 v220, v64, v65
	ds_read_b128 v[180:183], v210 offset:53248
	ds_write_b64 v229, v[144:145] offset:16384
	s_waitcnt lgkmcnt(9)
	v_mfma_f32_16x16x32_bf16 v[76:79], v[230:233], v[124:127], v[76:79]
	v_add_f32_e32 v221, v68, v69
	v_mfma_f32_16x16x32_bf16 v[72:75], v[230:233], v[108:111], v[72:75]
	v_add_f32_e32 v220, v220, v66
	ds_read_b128 v[230:233], v246 offset:8192
	v_mfma_f32_16x16x32_bf16 v[60:63], v[234:237], v[238:241], v[60:63]
	v_add_f32_e32 v221, v221, v70
	v_add_f32_e32 v220, v220, v67
	v_mfma_f32_16x16x32_bf16 v[56:59], v[234:237], v[216:219], v[56:59]
	v_add_f32_e32 v221, v221, v71
	ds_read_b128 v[234:237], v210 offset:55296
	s_waitcnt lgkmcnt(8)
	v_mfma_f32_16x16x32_bf16 v[80:83], v[160:163], v[96:99], 0
	v_exp_f32_e32 v72, v72
	v_mfma_f32_16x16x32_bf16 v[84:87], v[160:163], v[112:115], 0
	v_exp_f32_e32 v76, v76
	ds_read_b128 v[160:163], v201 offset:12288
	ds_write_b64 v184, v[146:147] offset:16384
	v_mfma_f32_16x16x32_bf16 v[0:3], v[164:167], v[242:245], v[0:3]
	v_exp_f32_e32 v73, v73
	v_mfma_f32_16x16x32_bf16 v[4:7], v[164:167], v[204:207], v[4:7]
	v_exp_f32_e32 v77, v77
	ds_read_b128 v[164:167], v210 offset:57344
	s_waitcnt lgkmcnt(8)
	v_mfma_f32_16x16x32_bf16 v[84:87], v[168:171], v[116:119], v[84:87]
	v_exp_f32_e32 v74, v74
	v_mfma_f32_16x16x32_bf16 v[80:83], v[168:171], v[100:103], v[80:83]
	v_exp_f32_e32 v78, v78
	ds_read_b128 v[168:171], v202 offset:12288
	v_mfma_f32_16x16x32_bf16 v[12:15], v[172:175], v[204:207], v[12:15]
	v_exp_f32_e32 v75, v75
	v_mfma_f32_16x16x32_bf16 v[8:11], v[172:175], v[242:245], v[8:11]
	v_exp_f32_e32 v79, v79
	ds_read_b128 v[172:175], v210 offset:59392
	global_load_dwordx4 v[148:151], v198, s[8:9]
	s_waitcnt lgkmcnt(8)
	v_mfma_f32_16x16x32_bf16 v[80:83], v[176:179], v[104:107], v[80:83]
	v_add_f32_e32 v220, v220, v72
	v_add_f32_e32 v221, v221, v76
	v_mfma_f32_16x16x32_bf16 v[84:87], v[176:179], v[120:123], v[84:87]
	v_add_f32_e32 v220, v220, v73
	ds_read_b128 v[176:179], v203 offset:12288
	v_mfma_f32_16x16x32_bf16 v[16:19], v[180:183], v[242:245], v[16:19]
	v_add_f32_e32 v221, v221, v77
	v_add_f32_e32 v220, v220, v74
	v_mfma_f32_16x16x32_bf16 v[20:23], v[180:183], v[204:207], v[20:23]
	v_add_f32_e32 v221, v221, v78
	ds_read_b128 v[180:183], v210 offset:61440
	s_waitcnt lgkmcnt(7)
	v_mfma_f32_16x16x32_bf16 v[84:87], v[230:233], v[124:127], v[84:87]
	v_add_f32_e32 v220, v220, v75
	v_add_f32_e32 v221, v221, v79
	v_mfma_f32_16x16x32_bf16 v[80:83], v[230:233], v[108:111], v[80:83]
	v_cvt_pk_bf16_f32 v216, v64, v65
	ds_read_b128 v[230:233], v246 offset:12288
	global_load_dwordx4 v[144:147], v199, s[8:9]
	v_mfma_f32_16x16x32_bf16 v[28:31], v[234:237], v[204:207], v[28:31]
	v_cvt_pk_bf16_f32 v217, v66, v67
	v_cvt_pk_bf16_f32 v238, v68, v69
	v_mfma_f32_16x16x32_bf16 v[24:27], v[234:237], v[242:245], v[24:27]
	v_cvt_pk_bf16_f32 v239, v70, v71
	ds_read_b128 v[234:237], v210 offset:63488
	s_waitcnt lgkmcnt(6)
	v_mfma_f32_16x16x32_bf16 v[88:91], v[160:163], v[96:99], 0
	v_exp_f32_e32 v80, v80
	v_mfma_f32_16x16x32_bf16 v[92:95], v[160:163], v[112:115], 0
	v_exp_f32_e32 v84, v84
	v_mfma_f32_16x16x32_bf16 v[32:35], v[164:167], v[242:245], v[32:35]
	v_exp_f32_e32 v81, v81
	v_mfma_f32_16x16x32_bf16 v[36:39], v[164:167], v[204:207], v[36:39]
	v_exp_f32_e32 v85, v85
	global_load_dwordx4 v[136:139], v196, s[6:7]
	s_waitcnt lgkmcnt(4)
	v_mfma_f32_16x16x32_bf16 v[92:95], v[168:171], v[116:119], v[92:95]
	v_exp_f32_e32 v82, v82
	v_mfma_f32_16x16x32_bf16 v[88:91], v[168:171], v[100:103], v[88:91]
	v_exp_f32_e32 v86, v86
	v_mfma_f32_16x16x32_bf16 v[44:47], v[172:175], v[204:207], v[44:47]
	v_exp_f32_e32 v83, v83
	v_mfma_f32_16x16x32_bf16 v[40:43], v[172:175], v[242:245], v[40:43]
	v_exp_f32_e32 v87, v87
	s_waitcnt lgkmcnt(3)
	v_mfma_f32_16x16x32_bf16 v[88:91], v[176:179], v[104:107], v[88:91]
	v_add_f32_e32 v220, v220, v80
	v_add_f32_e32 v221, v221, v84
	v_mfma_f32_16x16x32_bf16 v[92:95], v[176:179], v[120:123], v[92:95]
	v_add_f32_e32 v220, v220, v81
	global_load_dwordx4 v[140:143], v197, s[6:7]
	s_waitcnt lgkmcnt(0)
	s_barrier
	ds_read_b128 v[160:163], v201 offset:16384
	ds_read_b128 v[164:167], v209 offset:0
	ds_read_b128 v[168:171], v202 offset:16384
	ds_read_b128 v[172:175], v209 offset:2048
	ds_read_b128 v[176:179], v203 offset:16384
	v_mfma_f32_16x16x32_bf16 v[48:51], v[180:183], v[242:245], v[48:51]
	v_add_f32_e32 v221, v221, v85
	v_add_f32_e32 v220, v220, v82
	v_mfma_f32_16x16x32_bf16 v[52:55], v[180:183], v[204:207], v[52:55]
	v_add_f32_e32 v221, v221, v86
	ds_read_b128 v[180:183], v209 offset:4096
	v_mfma_f32_16x16x32_bf16 v[92:95], v[230:233], v[124:127], v[92:95]
	v_add_f32_e32 v220, v220, v83
	v_add_f32_e32 v221, v221, v87
	v_mfma_f32_16x16x32_bf16 v[88:91], v[230:233], v[108:111], v[88:91]
	v_cvt_pk_bf16_f32 v218, v72, v73
	ds_read_b128 v[230:233], v246 offset:16384
	s_add_u32 s10, s10, 0x200
	s_addc_u32 s11, s11, 0
	s_add_u32 s12, s12, 0x40000
	s_addc_u32 s13, s13, 0
	s_add_i32 s4, s4, 4
	s_cmpk_lt_u32 s4, 0x104
	s_cselect_b64 s[6:7], -1, 0
	s_and_b64 s[6:7], s[0:1], s[6:7]
	s_and_b64 vcc, exec, s[6:7]
	v_mfma_f32_16x16x32_bf16 v[60:63], v[234:237], v[204:207], v[60:63]
	v_cvt_pk_bf16_f32 v219, v74, v75
	v_cvt_pk_bf16_f32 v240, v76, v77
	v_mfma_f32_16x16x32_bf16 v[56:59], v[234:237], v[242:245], v[56:59]
	v_cvt_pk_bf16_f32 v241, v78, v79
	ds_read_b128 v[234:237], v209 offset:6144
	s_cbranch_vccnz .LBB0_734
	s_setprio 0
	s_waitcnt vmcnt(0)
	s_nop 7
	s_nop 7
	ds_swizzle_b32 v64, v194 offset:swizzle(SWAP,16)
	s_waitcnt lgkmcnt(0)
	v_add_f32_e32 v194, v194, v64
	v_mov_b32_e32 v65, v194
	s_nop 1
	v_permlane32_swap_b32_e32 v194, v65
	v_add_f32_e32 v194, v194, v65
	s_nop 0
	v_rcp_f32_e32 v66, v194
	ds_swizzle_b32 v64, v195 offset:swizzle(SWAP,16)
	s_waitcnt lgkmcnt(0)
	v_add_f32_e32 v195, v195, v64
	v_mov_b32_e32 v65, v195
	s_nop 1
	v_permlane32_swap_b32_e32 v195, v65
	v_add_f32_e32 v195, v195, v65
	s_nop 0
	v_rcp_f32_e32 v67, v195
	v_readlane_b32 s100, v250, 8
	v_mbcnt_lo_u32_b32 v68, -1, 0
	v_mbcnt_hi_u32_b32 v68, -1, v68
	v_and_b32_e32 v69, 15, v68
	v_lshrrev_b32_e32 v70, 4, v68
	s_lshr_b32 s101, s100, 1
	v_add_u32_e32 v69, s101, v69
	v_lshlrev_b32_e32 v69, 12, v69
	v_and_b32_e32 v71, 1, v70
	v_lshlrev_b32_e32 v71, 5, v71
	v_and_b32_e32 v70, 2, v70
	v_lshl_add_u32 v71, v70, 3, v71
	v_add_u32_e32 v70, v69, v71
	v_add_u32_e32 v71, 0x10000, v70
	v_mul_f32_e32 v0, v0, v66
	v_mul_f32_e32 v1, v1, v66
	v_mul_f32_e32 v2, v2, v66
	v_mul_f32_e32 v3, v3, v66
	v_mul_f32_e32 v8, v8, v66
	v_mul_f32_e32 v9, v9, v66
	v_mul_f32_e32 v10, v10, v66
	v_mul_f32_e32 v11, v11, v66
	v_cvt_pk_bf16_f32 v72, v0, v1
	v_cvt_pk_bf16_f32 v73, v2, v3
	v_cvt_pk_bf16_f32 v74, v8, v9
	v_cvt_pk_bf16_f32 v75, v10, v11
	s_nop 1
	v_permlane16_swap_b32_e32 v72, v74
	v_permlane16_swap_b32_e32 v73, v75
	s_nop 1
	global_store_dwordx4 v70, v[72:75], s[58:59] offset:0
	v_mul_f32_e32 v16, v16, v66
	v_mul_f32_e32 v17, v17, v66
	v_mul_f32_e32 v18, v18, v66
	v_mul_f32_e32 v19, v19, v66
	v_mul_f32_e32 v24, v24, v66
	v_mul_f32_e32 v25, v25, v66
	v_mul_f32_e32 v26, v26, v66
	v_mul_f32_e32 v27, v27, v66
	v_cvt_pk_bf16_f32 v76, v16, v17
	v_cvt_pk_bf16_f32 v77, v18, v19
	v_cvt_pk_bf16_f32 v78, v24, v25
	v_cvt_pk_bf16_f32 v79, v26, v27
	s_nop 1
	v_permlane16_swap_b32_e32 v76, v78
	v_permlane16_swap_b32_e32 v77, v79
	s_nop 1
	global_store_dwordx4 v70, v[76:79], s[58:59] offset:64
	v_mul_f32_e32 v32, v32, v66
	v_mul_f32_e32 v33, v33, v66
	v_mul_f32_e32 v34, v34, v66
	v_mul_f32_e32 v35, v35, v66
	v_mul_f32_e32 v40, v40, v66
	v_mul_f32_e32 v41, v41, v66
	v_mul_f32_e32 v42, v42, v66
	v_mul_f32_e32 v43, v43, v66
	v_cvt_pk_bf16_f32 v80, v32, v33
	v_cvt_pk_bf16_f32 v81, v34, v35
	v_cvt_pk_bf16_f32 v82, v40, v41
	v_cvt_pk_bf16_f32 v83, v42, v43
	s_nop 1
	v_permlane16_swap_b32_e32 v80, v82
	v_permlane16_swap_b32_e32 v81, v83
	s_nop 1
	global_store_dwordx4 v70, v[80:83], s[58:59] offset:128
	v_mul_f32_e32 v48, v48, v66
	v_mul_f32_e32 v49, v49, v66
	v_mul_f32_e32 v50, v50, v66
	v_mul_f32_e32 v51, v51, v66
	v_mul_f32_e32 v56, v56, v66
	v_mul_f32_e32 v57, v57, v66
	v_mul_f32_e32 v58, v58, v66
	v_mul_f32_e32 v59, v59, v66
	v_cvt_pk_bf16_f32 v84, v48, v49
	v_cvt_pk_bf16_f32 v85, v50, v51
	v_cvt_pk_bf16_f32 v86, v56, v57
	v_cvt_pk_bf16_f32 v87, v58, v59
	s_nop 1
	v_permlane16_swap_b32_e32 v84, v86
	v_permlane16_swap_b32_e32 v85, v87
	s_nop 1
	global_store_dwordx4 v70, v[84:87], s[58:59] offset:192
	v_mul_f32_e32 v4, v4, v67
	v_mul_f32_e32 v5, v5, v67
	v_mul_f32_e32 v6, v6, v67
	v_mul_f32_e32 v7, v7, v67
	v_mul_f32_e32 v12, v12, v67
	v_mul_f32_e32 v13, v13, v67
	v_mul_f32_e32 v14, v14, v67
	v_mul_f32_e32 v15, v15, v67
	v_cvt_pk_bf16_f32 v88, v4, v5
	v_cvt_pk_bf16_f32 v89, v6, v7
	v_cvt_pk_bf16_f32 v90, v12, v13
	v_cvt_pk_bf16_f32 v91, v14, v15
	s_nop 1
	v_permlane16_swap_b32_e32 v88, v90
	v_permlane16_swap_b32_e32 v89, v91
	s_nop 1
	global_store_dwordx4 v71, v[88:91], s[58:59] offset:0
	v_mul_f32_e32 v20, v20, v67
	v_mul_f32_e32 v21, v21, v67
	v_mul_f32_e32 v22, v22, v67
	v_mul_f32_e32 v23, v23, v67
	v_mul_f32_e32 v28, v28, v67
	v_mul_f32_e32 v29, v29, v67
	v_mul_f32_e32 v30, v30, v67
	v_mul_f32_e32 v31, v31, v67
	v_cvt_pk_bf16_f32 v92, v20, v21
	v_cvt_pk_bf16_f32 v93, v22, v23
	v_cvt_pk_bf16_f32 v94, v28, v29
	v_cvt_pk_bf16_f32 v95, v30, v31
	s_nop 1
	v_permlane16_swap_b32_e32 v92, v94
	v_permlane16_swap_b32_e32 v93, v95
	s_nop 1
	global_store_dwordx4 v71, v[92:95], s[58:59] offset:64
	v_mul_f32_e32 v36, v36, v67
	v_mul_f32_e32 v37, v37, v67
	v_mul_f32_e32 v38, v38, v67
	v_mul_f32_e32 v39, v39, v67
	v_mul_f32_e32 v44, v44, v67
	v_mul_f32_e32 v45, v45, v67
	v_mul_f32_e32 v46, v46, v67
	v_mul_f32_e32 v47, v47, v67
	v_cvt_pk_bf16_f32 v72, v36, v37
	v_cvt_pk_bf16_f32 v73, v38, v39
	v_cvt_pk_bf16_f32 v74, v44, v45
	v_cvt_pk_bf16_f32 v75, v46, v47
	s_nop 1
	v_permlane16_swap_b32_e32 v72, v74
	v_permlane16_swap_b32_e32 v73, v75
	s_nop 1
	global_store_dwordx4 v71, v[72:75], s[58:59] offset:128
	v_mul_f32_e32 v52, v52, v67
	v_mul_f32_e32 v53, v53, v67
	v_mul_f32_e32 v54, v54, v67
	v_mul_f32_e32 v55, v55, v67
	v_mul_f32_e32 v60, v60, v67
	v_mul_f32_e32 v61, v61, v67
	v_mul_f32_e32 v62, v62, v67
	v_mul_f32_e32 v63, v63, v67
	v_cvt_pk_bf16_f32 v76, v52, v53
	v_cvt_pk_bf16_f32 v77, v54, v55
	v_cvt_pk_bf16_f32 v78, v60, v61
	v_cvt_pk_bf16_f32 v79, v62, v63
	s_nop 1
	v_permlane16_swap_b32_e32 v76, v78
	v_permlane16_swap_b32_e32 v77, v79
	s_nop 1
	global_store_dwordx4 v71, v[76:79], s[58:59] offset:192
	s_barrier
